# z1 + phases A, C, F: first K-iteration peeled, its first-touch MFMAs take C=0, per-unit accumulator zeroing removed
# baseline (speedup 1.0000x reference)
.LBB0_197:
	s_add_u32 s3, s20, 0x100
	s_addc_u32 s46, s21, 0
	s_add_u32 s18, s18, 0x80080
	v_mov_b32_e32 v4, 0
	s_addc_u32 s19, s19, 0
	s_mov_b32 s48, -2
	s_add_u32 s20, s18, 0xfff80080
	s_addc_u32 s21, s19, -1
	s_add_i32 s49, 0, 0x10000
	s_cmp_eq_u32 s48, 28
	s_cselect_b32 s23, s15, s21
	s_cselect_b32 s22, s14, s20
	v_add_u32_e32 v2, s49, v1
	s_cselect_b32 s21, s17, s46
	s_cselect_b32 s20, s16, s3
	s_add_i32 s60, 0, 0x14000
	ds_read_b128 v[146:149], v2
	ds_read_b128 v[150:153], v2 offset:1024
	ds_read_b128 v[154:157], v2 offset:2048
	ds_read_b128 v[158:161], v2 offset:3072
	v_add_u32_e32 v2, s60, v1
	ds_read_b128 v[162:165], v2
	ds_read_b128 v[166:169], v2 offset:1024
	ds_read_b128 v[170:173], v2 offset:2048
	ds_read_b128 v[174:177], v2 offset:3072
	v_lshl_add_u64 v[194:195], s[18:19], 0, v[144:145]
	s_add_i32 m0, s34, 0xc000
	ds_read_b128 v[178:181], v133
	ds_read_b128 v[182:185], v133 offset:1024
	ds_read_b128 v[186:189], v133 offset:2048
	ds_read_b128 v[190:193], v133 offset:3072
	ds_read_b128 v[204:207], v133 offset:4096
	ds_read_b128 v[208:211], v133 offset:5120
	ds_read_b128 v[212:215], v133 offset:6144
	ds_read_b128 v[226:229], v133 offset:7168
	global_load_lds_dwordx4 v[194:195], off
	v_lshl_add_u64 v[194:195], s[18:19], 0, v[142:143]
	s_add_i32 m0, s34, 0xe000
	s_nop 0
	global_load_lds_dwordx4 v[194:195], off
	s_waitcnt vmcnt(8)
	s_waitcnt lgkmcnt(0)
	s_barrier
	s_setprio 1
	s_waitcnt lgkmcnt(0)
	v_mfma_f32_16x16x32_bf16 v[128:131], v[146:149], v[178:181], 0
	v_mfma_f32_16x16x32_bf16 v[124:127], v[154:157], v[178:181], 0
	v_mfma_f32_16x16x32_bf16 v[112:115], v[146:149], v[186:189], 0
	v_mfma_f32_16x16x32_bf16 v[108:111], v[154:157], v[186:189], 0
	v_mfma_f32_16x16x32_bf16 v[96:99], v[146:149], v[204:207], 0
	v_mfma_f32_16x16x32_bf16 v[92:95], v[154:157], v[204:207], 0
	v_mfma_f32_16x16x32_bf16 v[80:83], v[146:149], v[212:215], 0
	v_mfma_f32_16x16x32_bf16 v[76:79], v[154:157], v[212:215], 0
	v_mfma_f32_16x16x32_bf16 v[128:131], v[150:153], v[182:185], v[128:131]
	v_mfma_f32_16x16x32_bf16 v[124:127], v[158:161], v[182:185], v[124:127]
	v_mfma_f32_16x16x32_bf16 v[112:115], v[150:153], v[190:193], v[112:115]
	v_mfma_f32_16x16x32_bf16 v[108:111], v[158:161], v[190:193], v[108:111]
	v_mfma_f32_16x16x32_bf16 v[96:99], v[150:153], v[208:211], v[96:99]
	v_mfma_f32_16x16x32_bf16 v[92:95], v[158:161], v[208:211], v[92:95]
	v_mfma_f32_16x16x32_bf16 v[80:83], v[150:153], v[226:229], v[80:83]
	v_mfma_f32_16x16x32_bf16 v[76:79], v[158:161], v[226:229], v[76:79]
	s_setprio 0
	s_setprio 1
	v_mfma_f32_16x16x32_bf16 v[120:123], v[162:165], v[178:181], 0
	v_mfma_f32_16x16x32_bf16 v[116:119], v[170:173], v[178:181], 0
	v_mfma_f32_16x16x32_bf16 v[104:107], v[162:165], v[186:189], 0
	v_mfma_f32_16x16x32_bf16 v[100:103], v[170:173], v[186:189], 0
	v_mfma_f32_16x16x32_bf16 v[88:91], v[162:165], v[204:207], 0
	v_mfma_f32_16x16x32_bf16 v[84:87], v[170:173], v[204:207], 0
	v_mfma_f32_16x16x32_bf16 v[72:75], v[162:165], v[212:215], 0
	v_mfma_f32_16x16x32_bf16 v[68:71], v[170:173], v[212:215], 0
	v_mfma_f32_16x16x32_bf16 v[120:123], v[166:169], v[182:185], v[120:123]
	v_mfma_f32_16x16x32_bf16 v[116:119], v[174:177], v[182:185], v[116:119]
	v_mfma_f32_16x16x32_bf16 v[104:107], v[166:169], v[190:193], v[104:107]
	v_mfma_f32_16x16x32_bf16 v[100:103], v[174:177], v[190:193], v[100:103]
	v_mfma_f32_16x16x32_bf16 v[88:91], v[166:169], v[208:211], v[88:91]
	v_mfma_f32_16x16x32_bf16 v[84:87], v[174:177], v[208:211], v[84:87]
	v_mfma_f32_16x16x32_bf16 v[72:75], v[166:169], v[226:229], v[72:75]
	v_mfma_f32_16x16x32_bf16 v[68:71], v[174:177], v[226:229], v[68:71]
	s_setprio 0
	s_barrier
	s_add_i32 s49, s49, s31
	v_lshl_add_u64 v[194:195], s[20:21], 0, v[134:135]
	s_mov_b32 m0, s49
	ds_read_b128 v[178:181], v133 offset:16384
	ds_read_b128 v[182:185], v133 offset:17408
	ds_read_b128 v[186:189], v133 offset:18432
	ds_read_b128 v[190:193], v133 offset:19456
	ds_read_b128 v[204:207], v133 offset:20480
	ds_read_b128 v[208:211], v133 offset:21504
	ds_read_b128 v[212:215], v133 offset:22528
	ds_read_b128 v[226:229], v133 offset:23552
	global_load_lds_dwordx4 v[194:195], off
	s_add_i32 m0, s49, 0x2000
	s_add_u32 s58, s20, 0x80000
	v_lshl_add_u64 v[230:231], s[20:21], 0, v[138:139]
	s_addc_u32 s59, s21, 0
	s_add_i32 s49, s60, s31
	global_load_lds_dwordx4 v[230:231], off
	v_lshl_add_u64 v[232:233], s[58:59], 0, v[134:135]
	s_mov_b32 m0, s49
	v_lshl_add_u64 v[234:235], s[22:23], 0, v[140:141]
	global_load_lds_dwordx4 v[232:233], off
	v_lshl_add_u64 v[232:233], s[58:59], 0, v[138:139]
	s_add_i32 m0, s49, 0x2000
	s_nop 0
	global_load_lds_dwordx4 v[232:233], off
	v_lshl_add_u64 v[232:233], s[22:23], 0, v[136:137]
	s_mov_b32 m0, s34
	s_nop 0
	global_load_lds_dwordx4 v[232:233], off
	s_mov_b32 m0, s35
	s_nop 0
	global_load_lds_dwordx4 v[234:235], off
	s_waitcnt vmcnt(8)
	s_waitcnt lgkmcnt(0)
	s_barrier
	s_setprio 1
	s_waitcnt lgkmcnt(0)
	v_mfma_f32_16x16x32_bf16 v[64:67], v[146:149], v[178:181], 0
	v_mfma_f32_16x16x32_bf16 v[60:63], v[154:157], v[178:181], 0
	v_mfma_f32_16x16x32_bf16 v[48:51], v[146:149], v[186:189], 0
	v_mfma_f32_16x16x32_bf16 v[44:47], v[154:157], v[186:189], 0
	v_mfma_f32_16x16x32_bf16 v[32:35], v[146:149], v[204:207], 0
	v_mfma_f32_16x16x32_bf16 v[28:31], v[154:157], v[204:207], 0
	v_mfma_f32_16x16x32_bf16 v[16:19], v[146:149], v[212:215], 0
	v_mfma_f32_16x16x32_bf16 v[12:15], v[154:157], v[212:215], 0
	v_mfma_f32_16x16x32_bf16 v[64:67], v[150:153], v[182:185], v[64:67]
	v_mfma_f32_16x16x32_bf16 v[60:63], v[158:161], v[182:185], v[60:63]
	v_mfma_f32_16x16x32_bf16 v[48:51], v[150:153], v[190:193], v[48:51]
	v_mfma_f32_16x16x32_bf16 v[44:47], v[158:161], v[190:193], v[44:47]
	v_mfma_f32_16x16x32_bf16 v[32:35], v[150:153], v[208:211], v[32:35]
	v_mfma_f32_16x16x32_bf16 v[28:31], v[158:161], v[208:211], v[28:31]
	v_mfma_f32_16x16x32_bf16 v[16:19], v[150:153], v[226:229], v[16:19]
	v_mfma_f32_16x16x32_bf16 v[12:15], v[158:161], v[226:229], v[12:15]
	s_setprio 0
	s_setprio 1
	v_mfma_f32_16x16x32_bf16 v[56:59], v[162:165], v[178:181], 0
	v_mfma_f32_16x16x32_bf16 v[52:55], v[170:173], v[178:181], 0
	v_mfma_f32_16x16x32_bf16 v[40:43], v[162:165], v[186:189], 0
	v_mfma_f32_16x16x32_bf16 v[36:39], v[170:173], v[186:189], 0
	v_mfma_f32_16x16x32_bf16 v[24:27], v[162:165], v[204:207], 0
	v_mfma_f32_16x16x32_bf16 v[20:23], v[170:173], v[204:207], 0
	v_mfma_f32_16x16x32_bf16 v[8:11], v[162:165], v[212:215], 0
	v_mfma_f32_16x16x32_bf16 v[4:7], v[170:173], v[212:215], 0
	v_mfma_f32_16x16x32_bf16 v[56:59], v[166:169], v[182:185], v[56:59]
	v_mfma_f32_16x16x32_bf16 v[52:55], v[174:177], v[182:185], v[52:55]
	v_mfma_f32_16x16x32_bf16 v[40:43], v[166:169], v[190:193], v[40:43]
	v_mfma_f32_16x16x32_bf16 v[36:39], v[174:177], v[190:193], v[36:39]
	v_mfma_f32_16x16x32_bf16 v[24:27], v[166:169], v[208:211], v[24:27]
	v_mfma_f32_16x16x32_bf16 v[20:23], v[174:177], v[208:211], v[20:23]
	v_mfma_f32_16x16x32_bf16 v[8:11], v[166:169], v[226:229], v[8:11]
	v_mfma_f32_16x16x32_bf16 v[4:7], v[174:177], v[226:229], v[4:7]
	s_setprio 0
	s_barrier
	s_add_i32 s49, 0, 0x18000
	v_add_u32_e32 v2, s49, v1
	s_add_i32 s58, 0, 0x1c000
	ds_read_b128 v[146:149], v2
	ds_read_b128 v[150:153], v2 offset:1024
	ds_read_b128 v[154:157], v2 offset:2048
	ds_read_b128 v[158:161], v2 offset:3072
	v_add_u32_e32 v2, s58, v1
	ds_read_b128 v[162:165], v2
	ds_read_b128 v[166:169], v2 offset:1024
	ds_read_b128 v[170:173], v2 offset:2048
	ds_read_b128 v[174:177], v2 offset:3072
	s_add_u32 s22, s22, 0x80000
	s_addc_u32 s23, s23, 0
	s_mov_b32 m0, s36
	v_lshl_add_u64 v[236:237], s[22:23], 0, v[136:137]
	ds_read_b128 v[178:181], v133 offset:32768
	ds_read_b128 v[182:185], v133 offset:33792
	ds_read_b128 v[186:189], v133 offset:34816
	ds_read_b128 v[190:193], v133 offset:35840
	ds_read_b128 v[204:207], v133 offset:36864
	ds_read_b128 v[208:211], v133 offset:37888
	ds_read_b128 v[212:215], v133 offset:38912
	ds_read_b128 v[226:229], v133 offset:39936
	global_load_lds_dwordx4 v[236:237], off
	v_lshl_add_u64 v[236:237], s[22:23], 0, v[140:141]
	s_mov_b32 m0, s37
	s_nop 0
	global_load_lds_dwordx4 v[236:237], off
	s_waitcnt vmcnt(8)
	s_waitcnt lgkmcnt(0)
	s_barrier
	s_setprio 1
	s_waitcnt lgkmcnt(0)
	v_mfma_f32_16x16x32_bf16 v[128:131], v[146:149], v[178:181], v[128:131]
	v_mfma_f32_16x16x32_bf16 v[124:127], v[154:157], v[178:181], v[124:127]
	v_mfma_f32_16x16x32_bf16 v[112:115], v[146:149], v[186:189], v[112:115]
	v_mfma_f32_16x16x32_bf16 v[108:111], v[154:157], v[186:189], v[108:111]
	v_mfma_f32_16x16x32_bf16 v[96:99], v[146:149], v[204:207], v[96:99]
	v_mfma_f32_16x16x32_bf16 v[92:95], v[154:157], v[204:207], v[92:95]
	v_mfma_f32_16x16x32_bf16 v[80:83], v[146:149], v[212:215], v[80:83]
	v_mfma_f32_16x16x32_bf16 v[76:79], v[154:157], v[212:215], v[76:79]
	v_mfma_f32_16x16x32_bf16 v[128:131], v[150:153], v[182:185], v[128:131]
	v_mfma_f32_16x16x32_bf16 v[124:127], v[158:161], v[182:185], v[124:127]
	v_mfma_f32_16x16x32_bf16 v[112:115], v[150:153], v[190:193], v[112:115]
	v_mfma_f32_16x16x32_bf16 v[108:111], v[158:161], v[190:193], v[108:111]
	v_mfma_f32_16x16x32_bf16 v[96:99], v[150:153], v[208:211], v[96:99]
	v_mfma_f32_16x16x32_bf16 v[92:95], v[158:161], v[208:211], v[92:95]
	v_mfma_f32_16x16x32_bf16 v[80:83], v[150:153], v[226:229], v[80:83]
	v_mfma_f32_16x16x32_bf16 v[76:79], v[158:161], v[226:229], v[76:79]
	s_setprio 0
	s_setprio 1
	v_mfma_f32_16x16x32_bf16 v[120:123], v[162:165], v[178:181], v[120:123]
	v_mfma_f32_16x16x32_bf16 v[116:119], v[170:173], v[178:181], v[116:119]
	v_mfma_f32_16x16x32_bf16 v[104:107], v[162:165], v[186:189], v[104:107]
	v_mfma_f32_16x16x32_bf16 v[100:103], v[170:173], v[186:189], v[100:103]
	v_mfma_f32_16x16x32_bf16 v[88:91], v[162:165], v[204:207], v[88:91]
	v_mfma_f32_16x16x32_bf16 v[84:87], v[170:173], v[204:207], v[84:87]
	v_mfma_f32_16x16x32_bf16 v[72:75], v[162:165], v[212:215], v[72:75]
	v_mfma_f32_16x16x32_bf16 v[68:71], v[170:173], v[212:215], v[68:71]
	v_mfma_f32_16x16x32_bf16 v[120:123], v[166:169], v[182:185], v[120:123]
	v_mfma_f32_16x16x32_bf16 v[116:119], v[174:177], v[182:185], v[116:119]
	v_mfma_f32_16x16x32_bf16 v[104:107], v[166:169], v[190:193], v[104:107]
	v_mfma_f32_16x16x32_bf16 v[100:103], v[174:177], v[190:193], v[100:103]
	v_mfma_f32_16x16x32_bf16 v[88:91], v[166:169], v[208:211], v[88:91]
	v_mfma_f32_16x16x32_bf16 v[84:87], v[174:177], v[208:211], v[84:87]
	v_mfma_f32_16x16x32_bf16 v[72:75], v[166:169], v[226:229], v[72:75]
	v_mfma_f32_16x16x32_bf16 v[68:71], v[174:177], v[226:229], v[68:71]
	s_setprio 0
	s_barrier
	s_add_i32 s22, s49, s31
	v_lshl_add_u64 v[194:195], v[194:195], 0, s[94:95]
	s_mov_b32 m0, s22
	ds_read_b128 v[178:181], v133 offset:49152
	ds_read_b128 v[182:185], v133 offset:50176
	ds_read_b128 v[186:189], v133 offset:51200
	ds_read_b128 v[190:193], v133 offset:52224
	ds_read_b128 v[204:207], v133 offset:53248
	ds_read_b128 v[208:211], v133 offset:54272
	ds_read_b128 v[212:215], v133 offset:55296
	ds_read_b128 v[226:229], v133 offset:56320
	global_load_lds_dwordx4 v[194:195], off
	s_add_i32 m0, s22, 0x2000
	s_add_u32 s20, s20, 0x80080
	v_lshl_add_u64 v[194:195], v[230:231], 0, s[94:95]
	s_addc_u32 s21, s21, 0
	s_add_i32 s22, s58, s31
	global_load_lds_dwordx4 v[194:195], off
	v_lshl_add_u64 v[194:195], s[20:21], 0, v[134:135]
	s_mov_b32 m0, s22
	s_nop 0
	global_load_lds_dwordx4 v[194:195], off
	v_lshl_add_u64 v[194:195], s[20:21], 0, v[138:139]
	s_add_i32 m0, s22, 0x2000
	s_nop 0
	global_load_lds_dwordx4 v[194:195], off
	v_lshl_add_u64 v[194:195], v[232:233], 0, s[94:95]
	s_mov_b32 m0, s40
	s_nop 0
	global_load_lds_dwordx4 v[194:195], off
	v_lshl_add_u64 v[194:195], v[234:235], 0, s[94:95]
	s_mov_b32 m0, s41
	s_nop 0
	global_load_lds_dwordx4 v[194:195], off
	s_waitcnt vmcnt(8)
	s_waitcnt lgkmcnt(0)
	s_barrier
	s_setprio 1
	s_waitcnt lgkmcnt(0)
	v_mfma_f32_16x16x32_bf16 v[64:67], v[146:149], v[178:181], v[64:67]
	v_mfma_f32_16x16x32_bf16 v[60:63], v[154:157], v[178:181], v[60:63]
	v_mfma_f32_16x16x32_bf16 v[48:51], v[146:149], v[186:189], v[48:51]
	v_mfma_f32_16x16x32_bf16 v[44:47], v[154:157], v[186:189], v[44:47]
	v_mfma_f32_16x16x32_bf16 v[32:35], v[146:149], v[204:207], v[32:35]
	v_mfma_f32_16x16x32_bf16 v[28:31], v[154:157], v[204:207], v[28:31]
	v_mfma_f32_16x16x32_bf16 v[16:19], v[146:149], v[212:215], v[16:19]
	v_mfma_f32_16x16x32_bf16 v[12:15], v[154:157], v[212:215], v[12:15]
	v_mfma_f32_16x16x32_bf16 v[64:67], v[150:153], v[182:185], v[64:67]
	v_mfma_f32_16x16x32_bf16 v[60:63], v[158:161], v[182:185], v[60:63]
	v_mfma_f32_16x16x32_bf16 v[48:51], v[150:153], v[190:193], v[48:51]
	v_mfma_f32_16x16x32_bf16 v[44:47], v[158:161], v[190:193], v[44:47]
	v_mfma_f32_16x16x32_bf16 v[32:35], v[150:153], v[208:211], v[32:35]
	v_mfma_f32_16x16x32_bf16 v[28:31], v[158:161], v[208:211], v[28:31]
	v_mfma_f32_16x16x32_bf16 v[16:19], v[150:153], v[226:229], v[16:19]
	v_mfma_f32_16x16x32_bf16 v[12:15], v[158:161], v[226:229], v[12:15]
	s_setprio 0
	s_setprio 1
	v_mfma_f32_16x16x32_bf16 v[56:59], v[162:165], v[178:181], v[56:59]
	v_mfma_f32_16x16x32_bf16 v[52:55], v[170:173], v[178:181], v[52:55]
	v_mfma_f32_16x16x32_bf16 v[40:43], v[162:165], v[186:189], v[40:43]
	v_mfma_f32_16x16x32_bf16 v[36:39], v[170:173], v[186:189], v[36:39]
	v_mfma_f32_16x16x32_bf16 v[24:27], v[162:165], v[204:207], v[24:27]
	v_mfma_f32_16x16x32_bf16 v[20:23], v[170:173], v[204:207], v[20:23]
	v_mfma_f32_16x16x32_bf16 v[8:11], v[162:165], v[212:215], v[8:11]
	v_mfma_f32_16x16x32_bf16 v[4:7], v[170:173], v[212:215], v[4:7]
	v_mfma_f32_16x16x32_bf16 v[56:59], v[166:169], v[182:185], v[56:59]
	v_mfma_f32_16x16x32_bf16 v[52:55], v[174:177], v[182:185], v[52:55]
	v_mfma_f32_16x16x32_bf16 v[40:43], v[166:169], v[190:193], v[40:43]
	v_mfma_f32_16x16x32_bf16 v[36:39], v[174:177], v[190:193], v[36:39]
	v_mfma_f32_16x16x32_bf16 v[24:27], v[166:169], v[208:211], v[24:27]
	v_mfma_f32_16x16x32_bf16 v[20:23], v[174:177], v[208:211], v[20:23]
	v_mfma_f32_16x16x32_bf16 v[8:11], v[166:169], v[226:229], v[8:11]
	v_mfma_f32_16x16x32_bf16 v[4:7], v[174:177], v[226:229], v[4:7]
	s_setprio 0
	s_barrier
	s_add_i32 s48, s48, 2
	s_add_u32 s3, s3, 0x100
	s_addc_u32 s46, s46, 0
	s_add_u32 s18, s18, 0x100
	s_addc_u32 s19, s19, 0
	s_cmp_gt_u32 s48, 29
	s_cbranch_scc0 .LBB0_198

.LBB0_908:
	s_add_u32 s52, s22, 0x100
	s_addc_u32 s53, s23, 0
	s_add_u32 s4, s4, 0x80080
	v_mov_b32_e32 v4, 0
	s_addc_u32 s5, s5, 0
	s_mov_b32 s54, -2
	s_add_u32 s22, s4, 0xfff80080
	s_addc_u32 s23, s5, -1
	s_add_i32 s55, 0, 0x10000
	s_cmp_eq_u32 s54, 28
	s_cselect_b32 s25, s19, s23
	s_cselect_b32 s24, s18, s22
	v_add_u32_e32 v2, s55, v1
	s_cselect_b32 s23, s21, s53
	s_cselect_b32 s22, s20, s52
	s_add_i32 s58, 0, 0x14000
	ds_read_b128 v[132:135], v2
	ds_read_b128 v[136:139], v2 offset:1024
	ds_read_b128 v[152:155], v2 offset:2048
	ds_read_b128 v[156:159], v2 offset:3072
	v_add_u32_e32 v2, s58, v1
	ds_read_b128 v[164:167], v2
	ds_read_b128 v[168:171], v2 offset:1024
	ds_read_b128 v[172:175], v2 offset:2048
	ds_read_b128 v[176:179], v2 offset:3072
	v_lshl_add_u64 v[160:161], s[4:5], 0, v[150:151]
	s_add_i32 m0, s35, 0xc000
	ds_read_b128 v[180:183], v162
	ds_read_b128 v[184:187], v162 offset:1024
	ds_read_b128 v[188:191], v162 offset:2048
	ds_read_b128 v[192:195], v162 offset:3072
	ds_read_b128 v[204:207], v162 offset:4096
	ds_read_b128 v[208:211], v162 offset:5120
	ds_read_b128 v[212:215], v162 offset:6144
	ds_read_b128 v[226:229], v162 offset:7168
	global_load_lds_dwordx4 v[160:161], off
	v_lshl_add_u64 v[160:161], s[4:5], 0, v[148:149]
	s_add_i32 m0, s35, 0xe000
	s_nop 0
	global_load_lds_dwordx4 v[160:161], off
	s_waitcnt vmcnt(8)
	s_waitcnt lgkmcnt(0)
	s_barrier
	s_setprio 1
	s_waitcnt lgkmcnt(0)
	v_mfma_f32_16x16x32_bf16 v[128:131], v[132:135], v[180:183], 0
	v_mfma_f32_16x16x32_bf16 v[124:127], v[152:155], v[180:183], 0
	v_mfma_f32_16x16x32_bf16 v[112:115], v[132:135], v[188:191], 0
	v_mfma_f32_16x16x32_bf16 v[108:111], v[152:155], v[188:191], 0
	v_mfma_f32_16x16x32_bf16 v[96:99], v[132:135], v[204:207], 0
	v_mfma_f32_16x16x32_bf16 v[92:95], v[152:155], v[204:207], 0
	v_mfma_f32_16x16x32_bf16 v[80:83], v[132:135], v[212:215], 0
	v_mfma_f32_16x16x32_bf16 v[76:79], v[152:155], v[212:215], 0
	v_mfma_f32_16x16x32_bf16 v[128:131], v[136:139], v[184:187], v[128:131]
	v_mfma_f32_16x16x32_bf16 v[124:127], v[156:159], v[184:187], v[124:127]
	v_mfma_f32_16x16x32_bf16 v[112:115], v[136:139], v[192:195], v[112:115]
	v_mfma_f32_16x16x32_bf16 v[108:111], v[156:159], v[192:195], v[108:111]
	v_mfma_f32_16x16x32_bf16 v[96:99], v[136:139], v[208:211], v[96:99]
	v_mfma_f32_16x16x32_bf16 v[92:95], v[156:159], v[208:211], v[92:95]
	v_mfma_f32_16x16x32_bf16 v[80:83], v[136:139], v[226:229], v[80:83]
	v_mfma_f32_16x16x32_bf16 v[76:79], v[156:159], v[226:229], v[76:79]
	s_setprio 0
	s_setprio 1
	v_mfma_f32_16x16x32_bf16 v[120:123], v[164:167], v[180:183], 0
	v_mfma_f32_16x16x32_bf16 v[116:119], v[172:175], v[180:183], 0
	v_mfma_f32_16x16x32_bf16 v[104:107], v[164:167], v[188:191], 0
	v_mfma_f32_16x16x32_bf16 v[100:103], v[172:175], v[188:191], 0
	v_mfma_f32_16x16x32_bf16 v[88:91], v[164:167], v[204:207], 0
	v_mfma_f32_16x16x32_bf16 v[84:87], v[172:175], v[204:207], 0
	v_mfma_f32_16x16x32_bf16 v[72:75], v[164:167], v[212:215], 0
	v_mfma_f32_16x16x32_bf16 v[68:71], v[172:175], v[212:215], 0
	v_mfma_f32_16x16x32_bf16 v[120:123], v[168:171], v[184:187], v[120:123]
	v_mfma_f32_16x16x32_bf16 v[116:119], v[176:179], v[184:187], v[116:119]
	v_mfma_f32_16x16x32_bf16 v[104:107], v[168:171], v[192:195], v[104:107]
	v_mfma_f32_16x16x32_bf16 v[100:103], v[176:179], v[192:195], v[100:103]
	v_mfma_f32_16x16x32_bf16 v[88:91], v[168:171], v[208:211], v[88:91]
	v_mfma_f32_16x16x32_bf16 v[84:87], v[176:179], v[208:211], v[84:87]
	v_mfma_f32_16x16x32_bf16 v[72:75], v[168:171], v[226:229], v[72:75]
	v_mfma_f32_16x16x32_bf16 v[68:71], v[176:179], v[226:229], v[68:71]
	s_setprio 0
	s_barrier
	s_add_i32 s55, s55, s34
	v_lshl_add_u64 v[160:161], s[22:23], 0, v[140:141]
	s_mov_b32 m0, s55
	ds_read_b128 v[180:183], v162 offset:16384
	ds_read_b128 v[184:187], v162 offset:17408
	ds_read_b128 v[188:191], v162 offset:18432
	ds_read_b128 v[192:195], v162 offset:19456
	ds_read_b128 v[204:207], v162 offset:20480
	ds_read_b128 v[208:211], v162 offset:21504
	ds_read_b128 v[212:215], v162 offset:22528
	ds_read_b128 v[226:229], v162 offset:23552
	global_load_lds_dwordx4 v[160:161], off
	s_add_i32 m0, s55, 0x2000
	s_add_u32 s56, s22, 0x80000
	v_lshl_add_u64 v[230:231], s[22:23], 0, v[144:145]
	s_addc_u32 s57, s23, 0
	s_add_i32 s55, s58, s34
	global_load_lds_dwordx4 v[230:231], off
	v_lshl_add_u64 v[232:233], s[56:57], 0, v[140:141]
	s_mov_b32 m0, s55
	v_lshl_add_u64 v[234:235], s[24:25], 0, v[146:147]
	global_load_lds_dwordx4 v[232:233], off
	v_lshl_add_u64 v[232:233], s[56:57], 0, v[144:145]
	s_add_i32 m0, s55, 0x2000
	s_nop 0
	global_load_lds_dwordx4 v[232:233], off
	v_lshl_add_u64 v[232:233], s[24:25], 0, v[142:143]
	s_mov_b32 m0, s35
	s_nop 0
	global_load_lds_dwordx4 v[232:233], off
	s_mov_b32 m0, s36
	s_nop 0
	global_load_lds_dwordx4 v[234:235], off
	s_waitcnt vmcnt(8)
	s_waitcnt lgkmcnt(0)
	s_barrier
	s_setprio 1
	s_waitcnt lgkmcnt(0)
	v_mfma_f32_16x16x32_bf16 v[64:67], v[132:135], v[180:183], 0
	v_mfma_f32_16x16x32_bf16 v[60:63], v[152:155], v[180:183], 0
	v_mfma_f32_16x16x32_bf16 v[48:51], v[132:135], v[188:191], 0
	v_mfma_f32_16x16x32_bf16 v[44:47], v[152:155], v[188:191], 0
	v_mfma_f32_16x16x32_bf16 v[32:35], v[132:135], v[204:207], 0
	v_mfma_f32_16x16x32_bf16 v[28:31], v[152:155], v[204:207], 0
	v_mfma_f32_16x16x32_bf16 v[16:19], v[132:135], v[212:215], 0
	v_mfma_f32_16x16x32_bf16 v[12:15], v[152:155], v[212:215], 0
	v_mfma_f32_16x16x32_bf16 v[64:67], v[136:139], v[184:187], v[64:67]
	v_mfma_f32_16x16x32_bf16 v[60:63], v[156:159], v[184:187], v[60:63]
	v_mfma_f32_16x16x32_bf16 v[48:51], v[136:139], v[192:195], v[48:51]
	v_mfma_f32_16x16x32_bf16 v[44:47], v[156:159], v[192:195], v[44:47]
	v_mfma_f32_16x16x32_bf16 v[32:35], v[136:139], v[208:211], v[32:35]
	v_mfma_f32_16x16x32_bf16 v[28:31], v[156:159], v[208:211], v[28:31]
	v_mfma_f32_16x16x32_bf16 v[16:19], v[136:139], v[226:229], v[16:19]
	v_mfma_f32_16x16x32_bf16 v[12:15], v[156:159], v[226:229], v[12:15]
	s_setprio 0
	s_setprio 1
	v_mfma_f32_16x16x32_bf16 v[56:59], v[164:167], v[180:183], 0
	v_mfma_f32_16x16x32_bf16 v[52:55], v[172:175], v[180:183], 0
	v_mfma_f32_16x16x32_bf16 v[40:43], v[164:167], v[188:191], 0
	v_mfma_f32_16x16x32_bf16 v[36:39], v[172:175], v[188:191], 0
	v_mfma_f32_16x16x32_bf16 v[24:27], v[164:167], v[204:207], 0
	v_mfma_f32_16x16x32_bf16 v[20:23], v[172:175], v[204:207], 0
	v_mfma_f32_16x16x32_bf16 v[8:11], v[164:167], v[212:215], 0
	v_mfma_f32_16x16x32_bf16 v[4:7], v[172:175], v[212:215], 0
	v_mfma_f32_16x16x32_bf16 v[56:59], v[168:171], v[184:187], v[56:59]
	v_mfma_f32_16x16x32_bf16 v[52:55], v[176:179], v[184:187], v[52:55]
	v_mfma_f32_16x16x32_bf16 v[40:43], v[168:171], v[192:195], v[40:43]
	v_mfma_f32_16x16x32_bf16 v[36:39], v[176:179], v[192:195], v[36:39]
	v_mfma_f32_16x16x32_bf16 v[24:27], v[168:171], v[208:211], v[24:27]
	v_mfma_f32_16x16x32_bf16 v[20:23], v[176:179], v[208:211], v[20:23]
	v_mfma_f32_16x16x32_bf16 v[8:11], v[168:171], v[226:229], v[8:11]
	v_mfma_f32_16x16x32_bf16 v[4:7], v[176:179], v[226:229], v[4:7]
	s_setprio 0
	s_barrier
	s_add_i32 s55, 0, 0x18000
	v_add_u32_e32 v2, s55, v1
	s_add_i32 s56, 0, 0x1c000
	ds_read_b128 v[132:135], v2
	ds_read_b128 v[136:139], v2 offset:1024
	ds_read_b128 v[152:155], v2 offset:2048
	ds_read_b128 v[156:159], v2 offset:3072
	v_add_u32_e32 v2, s56, v1
	ds_read_b128 v[164:167], v2
	ds_read_b128 v[168:171], v2 offset:1024
	ds_read_b128 v[172:175], v2 offset:2048
	ds_read_b128 v[176:179], v2 offset:3072
	s_add_u32 s24, s24, 0x80000
	s_addc_u32 s25, s25, 0
	s_mov_b32 m0, s37
	v_lshl_add_u64 v[236:237], s[24:25], 0, v[142:143]
	ds_read_b128 v[180:183], v162 offset:32768
	ds_read_b128 v[184:187], v162 offset:33792
	ds_read_b128 v[188:191], v162 offset:34816
	ds_read_b128 v[192:195], v162 offset:35840
	ds_read_b128 v[204:207], v162 offset:36864
	ds_read_b128 v[208:211], v162 offset:37888
	ds_read_b128 v[212:215], v162 offset:38912
	ds_read_b128 v[226:229], v162 offset:39936
	global_load_lds_dwordx4 v[236:237], off
	v_lshl_add_u64 v[236:237], s[24:25], 0, v[146:147]
	s_mov_b32 m0, s38
	s_nop 0
	global_load_lds_dwordx4 v[236:237], off
	s_waitcnt vmcnt(8)
	s_waitcnt lgkmcnt(0)
	s_barrier
	s_setprio 1
	s_waitcnt lgkmcnt(0)
	v_mfma_f32_16x16x32_bf16 v[128:131], v[132:135], v[180:183], v[128:131]
	v_mfma_f32_16x16x32_bf16 v[124:127], v[152:155], v[180:183], v[124:127]
	v_mfma_f32_16x16x32_bf16 v[112:115], v[132:135], v[188:191], v[112:115]
	v_mfma_f32_16x16x32_bf16 v[108:111], v[152:155], v[188:191], v[108:111]
	v_mfma_f32_16x16x32_bf16 v[96:99], v[132:135], v[204:207], v[96:99]
	v_mfma_f32_16x16x32_bf16 v[92:95], v[152:155], v[204:207], v[92:95]
	v_mfma_f32_16x16x32_bf16 v[80:83], v[132:135], v[212:215], v[80:83]
	v_mfma_f32_16x16x32_bf16 v[76:79], v[152:155], v[212:215], v[76:79]
	v_mfma_f32_16x16x32_bf16 v[128:131], v[136:139], v[184:187], v[128:131]
	v_mfma_f32_16x16x32_bf16 v[124:127], v[156:159], v[184:187], v[124:127]
	v_mfma_f32_16x16x32_bf16 v[112:115], v[136:139], v[192:195], v[112:115]
	v_mfma_f32_16x16x32_bf16 v[108:111], v[156:159], v[192:195], v[108:111]
	v_mfma_f32_16x16x32_bf16 v[96:99], v[136:139], v[208:211], v[96:99]
	v_mfma_f32_16x16x32_bf16 v[92:95], v[156:159], v[208:211], v[92:95]
	v_mfma_f32_16x16x32_bf16 v[80:83], v[136:139], v[226:229], v[80:83]
	v_mfma_f32_16x16x32_bf16 v[76:79], v[156:159], v[226:229], v[76:79]
	s_setprio 0
	s_setprio 1
	v_mfma_f32_16x16x32_bf16 v[120:123], v[164:167], v[180:183], v[120:123]
	v_mfma_f32_16x16x32_bf16 v[116:119], v[172:175], v[180:183], v[116:119]
	v_mfma_f32_16x16x32_bf16 v[104:107], v[164:167], v[188:191], v[104:107]
	v_mfma_f32_16x16x32_bf16 v[100:103], v[172:175], v[188:191], v[100:103]
	v_mfma_f32_16x16x32_bf16 v[88:91], v[164:167], v[204:207], v[88:91]
	v_mfma_f32_16x16x32_bf16 v[84:87], v[172:175], v[204:207], v[84:87]
	v_mfma_f32_16x16x32_bf16 v[72:75], v[164:167], v[212:215], v[72:75]
	v_mfma_f32_16x16x32_bf16 v[68:71], v[172:175], v[212:215], v[68:71]
	v_mfma_f32_16x16x32_bf16 v[120:123], v[168:171], v[184:187], v[120:123]
	v_mfma_f32_16x16x32_bf16 v[116:119], v[176:179], v[184:187], v[116:119]
	v_mfma_f32_16x16x32_bf16 v[104:107], v[168:171], v[192:195], v[104:107]
	v_mfma_f32_16x16x32_bf16 v[100:103], v[176:179], v[192:195], v[100:103]
	v_mfma_f32_16x16x32_bf16 v[88:91], v[168:171], v[208:211], v[88:91]
	v_mfma_f32_16x16x32_bf16 v[84:87], v[176:179], v[208:211], v[84:87]
	v_mfma_f32_16x16x32_bf16 v[72:75], v[168:171], v[226:229], v[72:75]
	v_mfma_f32_16x16x32_bf16 v[68:71], v[176:179], v[226:229], v[68:71]
	s_setprio 0
	s_barrier
	s_add_i32 s24, s55, s34
	v_lshl_add_u64 v[160:161], v[160:161], 0, s[94:95]
	s_mov_b32 m0, s24
	ds_read_b128 v[180:183], v162 offset:49152
	ds_read_b128 v[184:187], v162 offset:50176
	ds_read_b128 v[188:191], v162 offset:51200
	ds_read_b128 v[192:195], v162 offset:52224
	ds_read_b128 v[204:207], v162 offset:53248
	ds_read_b128 v[208:211], v162 offset:54272
	ds_read_b128 v[212:215], v162 offset:55296
	ds_read_b128 v[226:229], v162 offset:56320
	global_load_lds_dwordx4 v[160:161], off
	s_add_i32 m0, s24, 0x2000
	s_add_u32 s22, s22, 0x80080
	v_lshl_add_u64 v[160:161], v[230:231], 0, s[94:95]
	s_addc_u32 s23, s23, 0
	s_add_i32 s24, s56, s34
	global_load_lds_dwordx4 v[160:161], off
	v_lshl_add_u64 v[160:161], s[22:23], 0, v[140:141]
	s_mov_b32 m0, s24
	s_nop 0
	global_load_lds_dwordx4 v[160:161], off
	v_lshl_add_u64 v[160:161], s[22:23], 0, v[144:145]
	s_add_i32 m0, s24, 0x2000
	s_nop 0
	global_load_lds_dwordx4 v[160:161], off
	v_lshl_add_u64 v[160:161], v[232:233], 0, s[94:95]
	s_mov_b32 m0, s42
	s_nop 0
	global_load_lds_dwordx4 v[160:161], off
	v_lshl_add_u64 v[160:161], v[234:235], 0, s[94:95]
	s_mov_b32 m0, s43
	s_nop 0
	global_load_lds_dwordx4 v[160:161], off
	s_waitcnt vmcnt(8)
	s_waitcnt lgkmcnt(0)
	s_barrier
	s_setprio 1
	s_waitcnt lgkmcnt(0)
	v_mfma_f32_16x16x32_bf16 v[64:67], v[132:135], v[180:183], v[64:67]
	v_mfma_f32_16x16x32_bf16 v[60:63], v[152:155], v[180:183], v[60:63]
	v_mfma_f32_16x16x32_bf16 v[48:51], v[132:135], v[188:191], v[48:51]
	v_mfma_f32_16x16x32_bf16 v[44:47], v[152:155], v[188:191], v[44:47]
	v_mfma_f32_16x16x32_bf16 v[32:35], v[132:135], v[204:207], v[32:35]
	v_mfma_f32_16x16x32_bf16 v[28:31], v[152:155], v[204:207], v[28:31]
	v_mfma_f32_16x16x32_bf16 v[16:19], v[132:135], v[212:215], v[16:19]
	v_mfma_f32_16x16x32_bf16 v[12:15], v[152:155], v[212:215], v[12:15]
	v_mfma_f32_16x16x32_bf16 v[64:67], v[136:139], v[184:187], v[64:67]
	v_mfma_f32_16x16x32_bf16 v[60:63], v[156:159], v[184:187], v[60:63]
	v_mfma_f32_16x16x32_bf16 v[48:51], v[136:139], v[192:195], v[48:51]
	v_mfma_f32_16x16x32_bf16 v[44:47], v[156:159], v[192:195], v[44:47]
	v_mfma_f32_16x16x32_bf16 v[32:35], v[136:139], v[208:211], v[32:35]
	v_mfma_f32_16x16x32_bf16 v[28:31], v[156:159], v[208:211], v[28:31]
	v_mfma_f32_16x16x32_bf16 v[16:19], v[136:139], v[226:229], v[16:19]
	v_mfma_f32_16x16x32_bf16 v[12:15], v[156:159], v[226:229], v[12:15]
	s_setprio 0
	s_setprio 1
	v_mfma_f32_16x16x32_bf16 v[56:59], v[164:167], v[180:183], v[56:59]
	v_mfma_f32_16x16x32_bf16 v[52:55], v[172:175], v[180:183], v[52:55]
	v_mfma_f32_16x16x32_bf16 v[40:43], v[164:167], v[188:191], v[40:43]
	v_mfma_f32_16x16x32_bf16 v[36:39], v[172:175], v[188:191], v[36:39]
	v_mfma_f32_16x16x32_bf16 v[24:27], v[164:167], v[204:207], v[24:27]
	v_mfma_f32_16x16x32_bf16 v[20:23], v[172:175], v[204:207], v[20:23]
	v_mfma_f32_16x16x32_bf16 v[8:11], v[164:167], v[212:215], v[8:11]
	v_mfma_f32_16x16x32_bf16 v[4:7], v[172:175], v[212:215], v[4:7]
	v_mfma_f32_16x16x32_bf16 v[56:59], v[168:171], v[184:187], v[56:59]
	v_mfma_f32_16x16x32_bf16 v[52:55], v[176:179], v[184:187], v[52:55]
	v_mfma_f32_16x16x32_bf16 v[40:43], v[168:171], v[192:195], v[40:43]
	v_mfma_f32_16x16x32_bf16 v[36:39], v[176:179], v[192:195], v[36:39]
	v_mfma_f32_16x16x32_bf16 v[24:27], v[168:171], v[208:211], v[24:27]
	v_mfma_f32_16x16x32_bf16 v[20:23], v[176:179], v[208:211], v[20:23]
	v_mfma_f32_16x16x32_bf16 v[8:11], v[168:171], v[226:229], v[8:11]
	v_mfma_f32_16x16x32_bf16 v[4:7], v[176:179], v[226:229], v[4:7]
	s_setprio 0
	s_barrier
	s_add_i32 s54, s54, 2
	s_add_u32 s52, s52, 0x100
	s_addc_u32 s53, s53, 0
	s_add_u32 s4, s4, 0x100
	s_addc_u32 s5, s5, 0
	s_cmp_gt_u32 s54, 29
	s_cbranch_scc0 .LBB0_909

.LBB0_2673:
	s_and_b64 s[34:35], s[22:23], exec
	v_mov_b32_e32 v4, 0
	s_cselect_b32 s19, s17, s27
	s_cselect_b32 s25, s16, s26
	s_cselect_b32 s46, s21, s29
	s_cselect_b32 s64, s20, s28
	s_mov_b64 s[36:37], -1
	s_mov_b64 s[34:35], 0
	s_add_u32 s40, s26, s34
	s_addc_u32 s41, s27, s35
	s_add_u32 s38, s40, 0x100
	s_addc_u32 s39, s41, 0
	v_cndmask_b32_e64 v2, 0, 1, s[36:37]
	s_and_b64 s[36:37], s[30:31], exec
	s_cselect_b32 s37, s19, s39
	s_cselect_b32 s36, s25, s38
	s_add_u32 s34, s28, s34
	s_addc_u32 s35, s29, s35
	s_add_u32 s34, s34, 0x100
	s_addc_u32 s35, s35, 0
	s_add_i32 s73, 0, 0x10000
	s_and_b64 s[30:31], s[30:31], exec
	s_cselect_b32 s39, s46, s35
	s_cselect_b32 s38, s64, s34
	s_add_i32 s31, 0, 0x14000
	s_add_u32 s42, s40, 0x10080
	s_addc_u32 s43, s41, 0
	s_add_i32 s72, s73, s53
	s_add_i32 m0, s54, 0xc000
	s_add_i32 s76, s54, 0xe000
	s_add_i32 s69, s72, 0x2000
	v_add_u32_e32 v144, s73, v1
	s_add_u32 s40, s38, 0x10000
	ds_read_b128 v[132:135], v144
	ds_read_b128 v[148:151], v144 offset:1024
	ds_read_b128 v[152:155], v144 offset:2048
	ds_read_b128 v[156:159], v144 offset:3072
	v_add_u32_e32 v144, s31, v1
	s_addc_u32 s41, s39, 0
	s_add_i32 s71, s31, s53
	ds_read_b128 v[160:163], v144
	ds_read_b128 v[164:167], v144 offset:1024
	ds_read_b128 v[168:171], v144 offset:2048
	ds_read_b128 v[172:175], v144 offset:3072
	s_add_i32 s70, s71, 0x2000
	s_add_i32 s68, 0, 0x18000
	s_add_i32 s67, 0, 0x1c000
	s_add_u32 s34, s36, 0x10000
	s_addc_u32 s35, s37, 0
	s_add_i32 s66, s68, s53
	s_add_i32 s65, s66, 0x2000
	s_add_u32 s30, s38, 0x10080
	s_addc_u32 s31, s39, 0
	s_add_i32 s75, s67, s53
	s_add_i32 s73, s75, 0x2000
	v_cmp_ne_u32_e32 vcc, 1, v2
	v_lshl_add_u64 v[144:145], s[42:43], 0, v[138:139]
	ds_read_b128 v[176:179], v146
	ds_read_b128 v[180:183], v146 offset:1024
	ds_read_b128 v[184:187], v146 offset:2048
	ds_read_b128 v[188:191], v146 offset:3072
	ds_read_b128 v[192:195], v146 offset:4096
	ds_read_b128 v[204:207], v146 offset:5120
	ds_read_b128 v[208:211], v146 offset:6144
	ds_read_b128 v[212:215], v146 offset:7168
	global_load_lds_dwordx4 v[144:145], off
	v_lshl_add_u64 v[144:145], s[42:43], 0, v[142:143]
	s_mov_b32 m0, s76
	s_nop 0
	global_load_lds_dwordx4 v[144:145], off
	s_waitcnt vmcnt(8)
	s_waitcnt lgkmcnt(0)
	s_barrier
	s_setprio 1
	s_waitcnt lgkmcnt(0)
	v_mfma_f32_16x16x32_bf16 v[128:131], v[132:135], v[176:179], 0
	v_mfma_f32_16x16x32_bf16 v[124:127], v[152:155], v[176:179], 0
	v_mfma_f32_16x16x32_bf16 v[116:119], v[132:135], v[184:187], 0
	v_mfma_f32_16x16x32_bf16 v[108:111], v[152:155], v[184:187], 0
	v_mfma_f32_16x16x32_bf16 v[100:103], v[132:135], v[192:195], 0
	v_mfma_f32_16x16x32_bf16 v[92:95], v[152:155], v[192:195], 0
	v_mfma_f32_16x16x32_bf16 v[84:87], v[132:135], v[208:211], 0
	v_mfma_f32_16x16x32_bf16 v[76:79], v[152:155], v[208:211], 0
	v_mfma_f32_16x16x32_bf16 v[128:131], v[148:151], v[180:183], v[128:131]
	v_mfma_f32_16x16x32_bf16 v[124:127], v[156:159], v[180:183], v[124:127]
	v_mfma_f32_16x16x32_bf16 v[116:119], v[148:151], v[188:191], v[116:119]
	v_mfma_f32_16x16x32_bf16 v[108:111], v[156:159], v[188:191], v[108:111]
	v_mfma_f32_16x16x32_bf16 v[100:103], v[148:151], v[204:207], v[100:103]
	v_mfma_f32_16x16x32_bf16 v[92:95], v[156:159], v[204:207], v[92:95]
	v_mfma_f32_16x16x32_bf16 v[84:87], v[148:151], v[212:215], v[84:87]
	v_mfma_f32_16x16x32_bf16 v[76:79], v[156:159], v[212:215], v[76:79]
	s_setprio 0
	s_setprio 1
	v_mfma_f32_16x16x32_bf16 v[120:123], v[160:163], v[176:179], 0
	v_mfma_f32_16x16x32_bf16 v[112:115], v[168:171], v[176:179], 0
	v_mfma_f32_16x16x32_bf16 v[104:107], v[160:163], v[184:187], 0
	v_mfma_f32_16x16x32_bf16 v[96:99], v[168:171], v[184:187], 0
	v_mfma_f32_16x16x32_bf16 v[88:91], v[160:163], v[192:195], 0
	v_mfma_f32_16x16x32_bf16 v[80:83], v[168:171], v[192:195], 0
	v_mfma_f32_16x16x32_bf16 v[72:75], v[160:163], v[208:211], 0
	v_mfma_f32_16x16x32_bf16 v[68:71], v[168:171], v[208:211], 0
	v_mfma_f32_16x16x32_bf16 v[120:123], v[164:167], v[180:183], v[120:123]
	v_mfma_f32_16x16x32_bf16 v[112:115], v[172:175], v[180:183], v[112:115]
	v_mfma_f32_16x16x32_bf16 v[104:107], v[164:167], v[188:191], v[104:107]
	v_mfma_f32_16x16x32_bf16 v[96:99], v[172:175], v[188:191], v[96:99]
	v_mfma_f32_16x16x32_bf16 v[88:91], v[164:167], v[204:207], v[88:91]
	v_mfma_f32_16x16x32_bf16 v[80:83], v[172:175], v[204:207], v[80:83]
	v_mfma_f32_16x16x32_bf16 v[72:75], v[164:167], v[212:215], v[72:75]
	v_mfma_f32_16x16x32_bf16 v[68:71], v[172:175], v[212:215], v[68:71]
	s_setprio 0
	s_barrier
	s_mov_b32 m0, s72
	v_lshl_add_u64 v[144:145], s[38:39], 0, v[136:137]
	ds_read_b128 v[176:179], v146 offset:16384
	ds_read_b128 v[180:183], v146 offset:17408
	ds_read_b128 v[184:187], v146 offset:18432
	ds_read_b128 v[188:191], v146 offset:19456
	ds_read_b128 v[192:195], v146 offset:20480
	ds_read_b128 v[204:207], v146 offset:21504
	ds_read_b128 v[208:211], v146 offset:22528
	ds_read_b128 v[212:215], v146 offset:23552
	global_load_lds_dwordx4 v[144:145], off
	v_lshl_add_u64 v[226:227], s[38:39], 0, v[140:141]
	s_mov_b32 m0, s69
	v_lshl_add_u64 v[228:229], s[40:41], 0, v[136:137]
	global_load_lds_dwordx4 v[226:227], off
	s_mov_b32 m0, s71
	v_lshl_add_u64 v[230:231], s[36:37], 0, v[142:143]
	global_load_lds_dwordx4 v[228:229], off
	v_lshl_add_u64 v[228:229], s[40:41], 0, v[140:141]
	s_mov_b32 m0, s70
	s_nop 0
	global_load_lds_dwordx4 v[228:229], off
	v_lshl_add_u64 v[228:229], s[36:37], 0, v[138:139]
	s_mov_b32 m0, s54
	s_nop 0
	global_load_lds_dwordx4 v[228:229], off
	s_mov_b32 m0, s55
	s_nop 0
	global_load_lds_dwordx4 v[230:231], off
	s_waitcnt vmcnt(8)
	s_waitcnt lgkmcnt(0)
	s_barrier
	s_setprio 1
	s_waitcnt lgkmcnt(0)
	v_mfma_f32_16x16x32_bf16 v[64:67], v[132:135], v[176:179], 0
	v_mfma_f32_16x16x32_bf16 v[60:63], v[152:155], v[176:179], 0
	v_mfma_f32_16x16x32_bf16 v[52:55], v[132:135], v[184:187], 0
	v_mfma_f32_16x16x32_bf16 v[44:47], v[152:155], v[184:187], 0
	v_mfma_f32_16x16x32_bf16 v[36:39], v[132:135], v[192:195], 0
	v_mfma_f32_16x16x32_bf16 v[28:31], v[152:155], v[192:195], 0
	v_mfma_f32_16x16x32_bf16 v[20:23], v[132:135], v[208:211], 0
	v_mfma_f32_16x16x32_bf16 v[12:15], v[152:155], v[208:211], 0
	v_mfma_f32_16x16x32_bf16 v[64:67], v[148:151], v[180:183], v[64:67]
	v_mfma_f32_16x16x32_bf16 v[60:63], v[156:159], v[180:183], v[60:63]
	v_mfma_f32_16x16x32_bf16 v[52:55], v[148:151], v[188:191], v[52:55]
	v_mfma_f32_16x16x32_bf16 v[44:47], v[156:159], v[188:191], v[44:47]
	v_mfma_f32_16x16x32_bf16 v[36:39], v[148:151], v[204:207], v[36:39]
	v_mfma_f32_16x16x32_bf16 v[28:31], v[156:159], v[204:207], v[28:31]
	v_mfma_f32_16x16x32_bf16 v[20:23], v[148:151], v[212:215], v[20:23]
	v_mfma_f32_16x16x32_bf16 v[12:15], v[156:159], v[212:215], v[12:15]
	s_setprio 0
	s_setprio 1
	v_mfma_f32_16x16x32_bf16 v[56:59], v[160:163], v[176:179], 0
	v_mfma_f32_16x16x32_bf16 v[48:51], v[168:171], v[176:179], 0
	v_mfma_f32_16x16x32_bf16 v[40:43], v[160:163], v[184:187], 0
	v_mfma_f32_16x16x32_bf16 v[32:35], v[168:171], v[184:187], 0
	v_mfma_f32_16x16x32_bf16 v[24:27], v[160:163], v[192:195], 0
	v_mfma_f32_16x16x32_bf16 v[16:19], v[168:171], v[192:195], 0
	v_mfma_f32_16x16x32_bf16 v[8:11], v[160:163], v[208:211], 0
	v_mfma_f32_16x16x32_bf16 v[4:7], v[168:171], v[208:211], 0
	v_mfma_f32_16x16x32_bf16 v[56:59], v[164:167], v[180:183], v[56:59]
	v_mfma_f32_16x16x32_bf16 v[48:51], v[172:175], v[180:183], v[48:51]
	v_mfma_f32_16x16x32_bf16 v[40:43], v[164:167], v[188:191], v[40:43]
	v_mfma_f32_16x16x32_bf16 v[32:35], v[172:175], v[188:191], v[32:35]
	v_mfma_f32_16x16x32_bf16 v[24:27], v[164:167], v[204:207], v[24:27]
	v_mfma_f32_16x16x32_bf16 v[16:19], v[172:175], v[204:207], v[16:19]
	v_mfma_f32_16x16x32_bf16 v[8:11], v[164:167], v[212:215], v[8:11]
	v_mfma_f32_16x16x32_bf16 v[4:7], v[172:175], v[212:215], v[4:7]
	s_setprio 0
	s_barrier
	v_add_u32_e32 v2, s68, v1
	ds_read_b128 v[132:135], v2
	ds_read_b128 v[148:151], v2 offset:1024
	ds_read_b128 v[152:155], v2 offset:2048
	ds_read_b128 v[156:159], v2 offset:3072
	v_add_u32_e32 v2, s67, v1
	ds_read_b128 v[160:163], v2
	ds_read_b128 v[164:167], v2 offset:1024
	ds_read_b128 v[168:171], v2 offset:2048
	ds_read_b128 v[172:175], v2 offset:3072
	s_mov_b32 m0, s56
	v_lshl_add_u64 v[232:233], s[34:35], 0, v[138:139]
	ds_read_b128 v[176:179], v146 offset:32768
	ds_read_b128 v[180:183], v146 offset:33792
	ds_read_b128 v[184:187], v146 offset:34816
	ds_read_b128 v[188:191], v146 offset:35840
	ds_read_b128 v[192:195], v146 offset:36864
	ds_read_b128 v[204:207], v146 offset:37888
	ds_read_b128 v[208:211], v146 offset:38912
	ds_read_b128 v[212:215], v146 offset:39936
	global_load_lds_dwordx4 v[232:233], off
	v_lshl_add_u64 v[232:233], s[34:35], 0, v[142:143]
	s_mov_b32 m0, s57
	s_nop 0
	global_load_lds_dwordx4 v[232:233], off
	s_waitcnt vmcnt(8)
	s_waitcnt lgkmcnt(0)
	s_barrier
	s_setprio 1
	s_waitcnt lgkmcnt(0)
	v_mfma_f32_16x16x32_bf16 v[128:131], v[132:135], v[176:179], v[128:131]
	v_mfma_f32_16x16x32_bf16 v[124:127], v[152:155], v[176:179], v[124:127]
	v_mfma_f32_16x16x32_bf16 v[116:119], v[132:135], v[184:187], v[116:119]
	v_mfma_f32_16x16x32_bf16 v[108:111], v[152:155], v[184:187], v[108:111]
	v_mfma_f32_16x16x32_bf16 v[100:103], v[132:135], v[192:195], v[100:103]
	v_mfma_f32_16x16x32_bf16 v[92:95], v[152:155], v[192:195], v[92:95]
	v_mfma_f32_16x16x32_bf16 v[84:87], v[132:135], v[208:211], v[84:87]
	v_mfma_f32_16x16x32_bf16 v[76:79], v[152:155], v[208:211], v[76:79]
	v_mfma_f32_16x16x32_bf16 v[128:131], v[148:151], v[180:183], v[128:131]
	v_mfma_f32_16x16x32_bf16 v[124:127], v[156:159], v[180:183], v[124:127]
	v_mfma_f32_16x16x32_bf16 v[116:119], v[148:151], v[188:191], v[116:119]
	v_mfma_f32_16x16x32_bf16 v[108:111], v[156:159], v[188:191], v[108:111]
	v_mfma_f32_16x16x32_bf16 v[100:103], v[148:151], v[204:207], v[100:103]
	v_mfma_f32_16x16x32_bf16 v[92:95], v[156:159], v[204:207], v[92:95]
	v_mfma_f32_16x16x32_bf16 v[84:87], v[148:151], v[212:215], v[84:87]
	v_mfma_f32_16x16x32_bf16 v[76:79], v[156:159], v[212:215], v[76:79]
	s_setprio 0
	s_setprio 1
	v_mfma_f32_16x16x32_bf16 v[120:123], v[160:163], v[176:179], v[120:123]
	v_mfma_f32_16x16x32_bf16 v[112:115], v[168:171], v[176:179], v[112:115]
	v_mfma_f32_16x16x32_bf16 v[104:107], v[160:163], v[184:187], v[104:107]
	v_mfma_f32_16x16x32_bf16 v[96:99], v[168:171], v[184:187], v[96:99]
	v_mfma_f32_16x16x32_bf16 v[88:91], v[160:163], v[192:195], v[88:91]
	v_mfma_f32_16x16x32_bf16 v[80:83], v[168:171], v[192:195], v[80:83]
	v_mfma_f32_16x16x32_bf16 v[72:75], v[160:163], v[208:211], v[72:75]
	v_mfma_f32_16x16x32_bf16 v[68:71], v[168:171], v[208:211], v[68:71]
	v_mfma_f32_16x16x32_bf16 v[120:123], v[164:167], v[180:183], v[120:123]
	v_mfma_f32_16x16x32_bf16 v[112:115], v[172:175], v[180:183], v[112:115]
	v_mfma_f32_16x16x32_bf16 v[104:107], v[164:167], v[188:191], v[104:107]
	v_mfma_f32_16x16x32_bf16 v[96:99], v[172:175], v[188:191], v[96:99]
	v_mfma_f32_16x16x32_bf16 v[88:91], v[164:167], v[204:207], v[88:91]
	v_mfma_f32_16x16x32_bf16 v[80:83], v[172:175], v[204:207], v[80:83]
	v_mfma_f32_16x16x32_bf16 v[72:75], v[164:167], v[212:215], v[72:75]
	v_mfma_f32_16x16x32_bf16 v[68:71], v[172:175], v[212:215], v[68:71]
	s_setprio 0
	s_barrier
	s_mov_b32 m0, s66
	v_lshl_add_u64 v[144:145], v[144:145], 0, s[94:95]
	ds_read_b128 v[176:179], v146 offset:49152
	ds_read_b128 v[180:183], v146 offset:50176
	ds_read_b128 v[184:187], v146 offset:51200
	ds_read_b128 v[188:191], v146 offset:52224
	ds_read_b128 v[192:195], v146 offset:53248
	ds_read_b128 v[204:207], v146 offset:54272
	ds_read_b128 v[208:211], v146 offset:55296
	ds_read_b128 v[212:215], v146 offset:56320
	global_load_lds_dwordx4 v[144:145], off
	v_lshl_add_u64 v[144:145], v[226:227], 0, s[94:95]
	s_mov_b32 m0, s65
	s_nop 0
	global_load_lds_dwordx4 v[144:145], off
	v_lshl_add_u64 v[144:145], s[30:31], 0, v[136:137]
	s_mov_b32 m0, s75
	s_nop 0
	global_load_lds_dwordx4 v[144:145], off
	v_lshl_add_u64 v[144:145], s[30:31], 0, v[140:141]
	s_mov_b32 m0, s73
	s_nop 0
	global_load_lds_dwordx4 v[144:145], off
	v_lshl_add_u64 v[144:145], v[228:229], 0, s[94:95]
	s_mov_b32 m0, s59
	s_nop 0
	global_load_lds_dwordx4 v[144:145], off
	v_lshl_add_u64 v[144:145], v[230:231], 0, s[94:95]
	s_mov_b32 m0, s60
	s_nop 0
	global_load_lds_dwordx4 v[144:145], off
	s_waitcnt vmcnt(8)
	s_waitcnt lgkmcnt(0)
	s_barrier
	s_setprio 1
	s_waitcnt lgkmcnt(0)
	v_mfma_f32_16x16x32_bf16 v[64:67], v[132:135], v[176:179], v[64:67]
	v_mfma_f32_16x16x32_bf16 v[60:63], v[152:155], v[176:179], v[60:63]
	v_mfma_f32_16x16x32_bf16 v[52:55], v[132:135], v[184:187], v[52:55]
	v_mfma_f32_16x16x32_bf16 v[44:47], v[152:155], v[184:187], v[44:47]
	v_mfma_f32_16x16x32_bf16 v[36:39], v[132:135], v[192:195], v[36:39]
	v_mfma_f32_16x16x32_bf16 v[28:31], v[152:155], v[192:195], v[28:31]
	v_mfma_f32_16x16x32_bf16 v[20:23], v[132:135], v[208:211], v[20:23]
	v_mfma_f32_16x16x32_bf16 v[12:15], v[152:155], v[208:211], v[12:15]
	v_mfma_f32_16x16x32_bf16 v[64:67], v[148:151], v[180:183], v[64:67]
	v_mfma_f32_16x16x32_bf16 v[60:63], v[156:159], v[180:183], v[60:63]
	v_mfma_f32_16x16x32_bf16 v[52:55], v[148:151], v[188:191], v[52:55]
	v_mfma_f32_16x16x32_bf16 v[44:47], v[156:159], v[188:191], v[44:47]
	v_mfma_f32_16x16x32_bf16 v[36:39], v[148:151], v[204:207], v[36:39]
	v_mfma_f32_16x16x32_bf16 v[28:31], v[156:159], v[204:207], v[28:31]
	v_mfma_f32_16x16x32_bf16 v[20:23], v[148:151], v[212:215], v[20:23]
	v_mfma_f32_16x16x32_bf16 v[12:15], v[156:159], v[212:215], v[12:15]
	s_setprio 0
	s_setprio 1
	v_mfma_f32_16x16x32_bf16 v[56:59], v[160:163], v[176:179], v[56:59]
	v_mfma_f32_16x16x32_bf16 v[48:51], v[168:171], v[176:179], v[48:51]
	v_mfma_f32_16x16x32_bf16 v[40:43], v[160:163], v[184:187], v[40:43]
	v_mfma_f32_16x16x32_bf16 v[32:35], v[168:171], v[184:187], v[32:35]
	v_mfma_f32_16x16x32_bf16 v[24:27], v[160:163], v[192:195], v[24:27]
	v_mfma_f32_16x16x32_bf16 v[16:19], v[168:171], v[192:195], v[16:19]
	v_mfma_f32_16x16x32_bf16 v[8:11], v[160:163], v[208:211], v[8:11]
	v_mfma_f32_16x16x32_bf16 v[4:7], v[168:171], v[208:211], v[4:7]
	v_mfma_f32_16x16x32_bf16 v[56:59], v[164:167], v[180:183], v[56:59]
	v_mfma_f32_16x16x32_bf16 v[48:51], v[172:175], v[180:183], v[48:51]
	v_mfma_f32_16x16x32_bf16 v[40:43], v[164:167], v[188:191], v[40:43]
	v_mfma_f32_16x16x32_bf16 v[32:35], v[172:175], v[188:191], v[32:35]
	v_mfma_f32_16x16x32_bf16 v[24:27], v[164:167], v[204:207], v[24:27]
	v_mfma_f32_16x16x32_bf16 v[16:19], v[172:175], v[204:207], v[16:19]
	v_mfma_f32_16x16x32_bf16 v[8:11], v[164:167], v[212:215], v[8:11]
	v_mfma_f32_16x16x32_bf16 v[4:7], v[172:175], v[212:215], v[4:7]
	s_setprio 0
	s_barrier
	s_mov_b64 s[36:37], 0
	s_mov_b64 s[30:31], -1
	s_mov_b64 s[34:35], 0x100
	s_cbranch_vccz .LBB0_2674
